# code placement trial (doc 9.3): MLA / differential / stick-breaking unit code shifted by 4 bytes, later code kept at the same byte phase
# speedup vs baseline: 1.0039x; 1.0035x over previous
; __device__ __forceinline__ void claim_fire(unsigned* ctr, int tid, int* pend) { if (tid == 0) *pend = (int)__hip_atomic_fetch_add(ctr, 1u, __ATOMIC_RELAXED, __HIP_MEMORY_SCOPE_AGENT); }
;     ...
;     const int* pos = (const int*)a->in[1];
;     unsigned* q0ctr = F.ctl + CW_QUEUE + ((l + qlo) * 8 + 0 + qs) * 64; unsigned* q1ctr = F.ctl + CW_QUEUE + ((l + qlo) * 8 + 1 + qs) * 64;
;     const bf16_t* QA = (const bf16_t*)(F.ws + WS_QA); const bf16_t* KAp = (const bf16_t*)(F.ws + WS_KA); const bf16_t* VAp = (const bf16_t*)(F.ws + WS_VA);
;     bf16_t* O = (bf16_t*)(F.ws + WS_O);
;     int pend = 0, lastm = 1 << 20;
;     at::claim_fire(q0ctr, F.tid, &pend);
; __global__ void __launch_bounds__(NTHR, 2) mk_fwd(Args args) {
;     ...
;         if (RUN(PH_ATTN1)) phase_attn1(lds, wv, l);
.LBB0_853:
	s_nop 0
	v_readlane_b32 s40, v254, 62
	s_cmp_ge_i32 s1, s40
	s_cselect_b64 s[2:3], -1, 0
	v_readlane_b32 s42, v255, 0
	v_readlane_b32 s43, v255, 1
	v_writelane_b32 v255, s2, 5
	v_readlane_b32 s41, v254, 63
	s_nop 0
	v_writelane_b32 v255, s3, 6
	s_and_b64 s[2:3], s[2:3], s[10:11]
	s_andn2_b64 vcc, exec, s[2:3]
	s_cbranch_vccnz .LBB0_1112
	v_readlane_b32 s24, v253, 0
	v_readlane_b32 s25, v253, 1
	s_mov_b64 s[2:3], s[24:25]
	s_load_dwordx2 s[50:51], s[2:3], 0xf0
	s_lshl_b32 s2, s72, 9
	s_mov_b32 s1, -1
	s_mov_b64 s[46:47], s[24:25]
	s_ashr_i32 s3, s2, 31
	s_load_dwordx2 s[6:7], s[46:47], 0x8
	s_waitcnt lgkmcnt(0)
	v_mbcnt_lo_u32_b32 v0, s1, 0
	s_lshl_b64 s[2:3], s[2:3], 2
	v_mbcnt_hi_u32_b32 v0, s1, v0
	s_waitcnt lgkmcnt(0)
	s_add_u32 s1, s50, s2
	s_addc_u32 s2, s51, s3
	s_add_u32 s52, s1, 0x3000
	v_readlane_b32 s1, v253, 8
	s_waitcnt vmcnt(0)
	v_mov_b32_e32 v164, 0
	s_addc_u32 s53, s2, 0
	v_cmp_eq_u32_e64 s[38:39], s1, v0
	s_and_saveexec_b64 s[10:11], s[38:39]
	s_cbranch_execz .LBB0_858
	s_mov_b64 s[16:17], exec
	v_mbcnt_lo_u32_b32 v0, s16, 0
	v_mbcnt_hi_u32_b32 v0, s17, v0
	v_cmp_eq_u32_e32 vcc, 0, v0
	s_and_saveexec_b64 s[14:15], vcc
	s_cbranch_execz .LBB0_857
	s_bcnt1_i32_b64 s1, s[16:17]
	v_mov_b32_e32 v1, s1
	global_atomic_add v1, v31, v1, s[52:53] sc0

; __device__ __forceinline__ void claim_fire(unsigned* ctr, int tid, int* pend) { if (tid == 0) *pend = (int)__hip_atomic_fetch_add(ctr, 1u, __ATOMIC_RELAXED, __HIP_MEMORY_SCOPE_AGENT); }
;     ...
;     at::claim_fire(q2ctr, F.tid, &pend);
.LBB0_1019:
	s_nop 0
	s_nop 0
	s_nop 0
	s_nop 0
	s_nop 0
	s_nop 0
	s_nop 0
	s_nop 0
	s_nop 0
	s_nop 0
	s_nop 0
	s_nop 0
	s_nop 0
	s_nop 0
	s_nop 0
	s_add_u32 s14, s52, 0x200
	s_addc_u32 s15, s53, 0
	v_writelane_b32 v255, s14, 3
	s_nop 1
	v_writelane_b32 v255, s15, 4
	s_and_saveexec_b64 s[14:15], s[38:39]
	s_cbranch_execz .LBB0_1023
	s_mov_b64 s[34:35], exec
	v_mbcnt_lo_u32_b32 v0, s34, 0
	v_mbcnt_hi_u32_b32 v0, s35, v0
	v_cmp_eq_u32_e32 vcc, 0, v0
	s_and_saveexec_b64 s[16:17], vcc
	s_cbranch_execz .LBB0_1022
	s_bcnt1_i32_b64 s3, s[34:35]
	v_readlane_b32 s20, v255, 3
	v_mov_b32_e32 v1, s3
	v_readlane_b32 s21, v255, 4
	s_nop 4
	global_atomic_add v1, v31, v1, s[20:21] sc0
